# E21: E19 + nt cache policy on combine X loads and X stores (X is next read a phase later)
# speedup vs baseline: 1.0111x; 1.0044x over previous
.LBB0_1862:
	v_lshlrev_b32_e32 v172, 16, v126
	v_and_b32_e32 v173, 0xffff0000, v126
	v_lshlrev_b32_e32 v126, 16, v127
	v_and_b32_e32 v127, 0xffff0000, v127
	v_pk_add_f32 v[172:173], v[172:173], 0 op_sel_hi:[1,0]
	v_lshlrev_b32_e32 v174, 16, v124
	v_and_b32_e32 v175, 0xffff0000, v124
	v_pk_add_f32 v[126:127], v[126:127], 0 op_sel_hi:[1,0]
	v_lshlrev_b32_e32 v124, 16, v125
	v_and_b32_e32 v125, 0xffff0000, v125
	v_pk_add_f32 v[172:173], v[172:173], v[174:175]
	v_lshlrev_b32_e32 v174, 16, v152
	v_and_b32_e32 v175, 0xffff0000, v152
	v_pk_add_f32 v[124:125], v[126:127], v[124:125]
	v_lshlrev_b32_e32 v126, 16, v153
	v_and_b32_e32 v127, 0xffff0000, v153
	v_lshlrev_b32_e32 v152, 16, v128
	v_and_b32_e32 v153, 0xffff0000, v128
	v_lshlrev_b32_e32 v128, 16, v129
	v_and_b32_e32 v129, 0xffff0000, v129
	v_pk_add_f32 v[172:173], v[172:173], v[174:175]
	v_lshlrev_b32_e32 v174, 16, v154
	v_and_b32_e32 v175, 0xffff0000, v154
	v_pk_add_f32 v[124:125], v[124:125], v[126:127]
	v_lshlrev_b32_e32 v126, 16, v155
	v_and_b32_e32 v127, 0xffff0000, v155
	v_pk_add_f32 v[152:153], v[152:153], 0 op_sel_hi:[1,0]
	v_lshlrev_b32_e32 v154, 16, v130
	v_and_b32_e32 v155, 0xffff0000, v130
	v_pk_add_f32 v[128:129], v[128:129], 0 op_sel_hi:[1,0]
	v_lshlrev_b32_e32 v130, 16, v131
	v_and_b32_e32 v131, 0xffff0000, v131
	v_pk_add_f32 v[152:153], v[152:153], v[154:155]
	v_lshlrev_b32_e32 v154, 16, v148
	v_and_b32_e32 v155, 0xffff0000, v148
	v_pk_add_f32 v[128:129], v[128:129], v[130:131]
	v_lshlrev_b32_e32 v130, 16, v149
	v_and_b32_e32 v131, 0xffff0000, v149
	v_lshlrev_b32_e32 v148, 16, v132
	v_and_b32_e32 v149, 0xffff0000, v132
	v_lshlrev_b32_e32 v132, 16, v133
	v_and_b32_e32 v133, 0xffff0000, v133
	v_pk_add_f32 v[152:153], v[152:153], v[154:155]
	v_lshlrev_b32_e32 v154, 16, v150
	v_and_b32_e32 v155, 0xffff0000, v150
	v_pk_add_f32 v[128:129], v[128:129], v[130:131]
	v_lshlrev_b32_e32 v130, 16, v151
	v_and_b32_e32 v131, 0xffff0000, v151
	v_pk_add_f32 v[148:149], v[148:149], 0 op_sel_hi:[1,0]
	v_lshlrev_b32_e32 v150, 16, v134
	v_and_b32_e32 v151, 0xffff0000, v134
	v_pk_add_f32 v[132:133], v[132:133], 0 op_sel_hi:[1,0]
	v_lshlrev_b32_e32 v134, 16, v135
	v_and_b32_e32 v135, 0xffff0000, v135
	v_pk_add_f32 v[148:149], v[148:149], v[150:151]
	v_lshlrev_b32_e32 v150, 16, v144
	v_and_b32_e32 v151, 0xffff0000, v144
	v_pk_add_f32 v[132:133], v[132:133], v[134:135]
	v_lshlrev_b32_e32 v134, 16, v145
	v_and_b32_e32 v135, 0xffff0000, v145
	v_lshlrev_b32_e32 v144, 16, v136
	v_and_b32_e32 v145, 0xffff0000, v136
	v_lshlrev_b32_e32 v136, 16, v137
	v_and_b32_e32 v137, 0xffff0000, v137
	v_pk_add_f32 v[148:149], v[148:149], v[150:151]
	v_lshlrev_b32_e32 v150, 16, v146
	v_and_b32_e32 v151, 0xffff0000, v146
	v_pk_add_f32 v[132:133], v[132:133], v[134:135]
	v_lshlrev_b32_e32 v134, 16, v147
	v_and_b32_e32 v135, 0xffff0000, v147
	v_pk_add_f32 v[144:145], v[144:145], 0 op_sel_hi:[1,0]
	v_lshlrev_b32_e32 v146, 16, v138
	v_and_b32_e32 v147, 0xffff0000, v138
	v_pk_add_f32 v[136:137], v[136:137], 0 op_sel_hi:[1,0]
	v_lshlrev_b32_e32 v138, 16, v139
	v_and_b32_e32 v139, 0xffff0000, v139
	v_pk_add_f32 v[144:145], v[144:145], v[146:147]
	v_lshlrev_b32_e32 v146, 16, v140
	v_and_b32_e32 v147, 0xffff0000, v140
	v_pk_add_f32 v[136:137], v[136:137], v[138:139]
	v_lshlrev_b32_e32 v138, 16, v141
	v_and_b32_e32 v139, 0xffff0000, v141
	v_pk_add_f32 v[144:145], v[144:145], v[146:147]
	v_lshlrev_b32_e32 v146, 16, v142
	v_and_b32_e32 v147, 0xffff0000, v142
	v_pk_add_f32 v[136:137], v[136:137], v[138:139]
	v_lshlrev_b32_e32 v138, 16, v143
	v_and_b32_e32 v139, 0xffff0000, v143
	v_lshlrev_b32_e32 v164, 16, v160
	v_and_b32_e32 v165, 0xffff0000, v160
	v_lshlrev_b32_e32 v160, 16, v161
	v_and_b32_e32 v161, 0xffff0000, v161
	v_lshlrev_b32_e32 v166, 16, v162
	v_and_b32_e32 v167, 0xffff0000, v162
	v_lshlrev_b32_e32 v162, 16, v163
	v_and_b32_e32 v163, 0xffff0000, v163
	v_lshlrev_b32_e32 v168, 16, v158
	v_and_b32_e32 v169, 0xffff0000, v158
	v_lshlrev_b32_e32 v158, 16, v159
	v_and_b32_e32 v159, 0xffff0000, v159
	v_lshlrev_b32_e32 v170, 16, v156
	v_and_b32_e32 v171, 0xffff0000, v156
	v_lshlrev_b32_e32 v156, 16, v157
	v_and_b32_e32 v157, 0xffff0000, v157
	v_pk_add_f32 v[172:173], v[172:173], v[174:175]
	v_pk_add_f32 v[126:127], v[124:125], v[126:127]
	v_pk_add_f32 v[152:153], v[152:153], v[154:155]
	v_pk_add_f32 v[130:131], v[128:129], v[130:131]
	v_pk_add_f32 v[148:149], v[148:149], v[150:151]
	v_pk_add_f32 v[134:135], v[132:133], v[134:135]
	v_pk_add_f32 v[144:145], v[144:145], v[146:147]
	v_pk_add_f32 v[138:139], v[136:137], v[138:139]
	s_waitcnt vmcnt(3)
	v_pk_fma_f32 v[124:125], v[172:173], v[50:51], v[164:165]
	v_pk_fma_f32 v[126:127], v[126:127], v[52:53], v[160:161]
	s_waitcnt vmcnt(2)
	v_pk_fma_f32 v[128:129], v[152:153], v[54:55], v[166:167]
	v_pk_fma_f32 v[130:131], v[130:131], v[56:57], v[162:163]
	s_waitcnt vmcnt(1)
	v_pk_fma_f32 v[132:133], v[148:149], v[58:59], v[168:169]
	v_pk_fma_f32 v[134:135], v[134:135], v[60:61], v[158:159]
	s_waitcnt vmcnt(0)
	v_pk_fma_f32 v[136:137], v[144:145], v[62:63], v[170:171]
	v_pk_fma_f32 v[138:139], v[138:139], v[64:65], v[156:157]
	s_and_b64 vcc, exec, s[8:9]
	v_lshl_add_u64 v[142:143], s[6:7], 0, v[74:75]
	s_cbranch_vccz .LBB0_1864
	v_add_co_u32_e32 v144, vcc, 0x33000000, v142
	v_cvt_pk_bf16_f32 v140, v124, v125
	v_cvt_pk_bf16_f32 v141, v126, v127
	v_addc_co_u32_e32 v145, vcc, 0, v143, vcc
	global_store_dwordx2 v[144:145], v[140:141], off nt
	v_cvt_pk_bf16_f32 v140, v128, v129
	v_cvt_pk_bf16_f32 v141, v130, v131
	global_store_dwordx2 v[144:145], v[140:141], off offset:512 nt
	v_cvt_pk_bf16_f32 v140, v132, v133
	v_cvt_pk_bf16_f32 v141, v134, v135
	global_store_dwordx2 v[144:145], v[140:141], off offset:1024 nt
	v_cvt_pk_bf16_f32 v140, v136, v137
	v_cvt_pk_bf16_f32 v141, v138, v139
	global_store_dwordx2 v[144:145], v[140:141], off offset:1536 nt
